# v15
# speedup vs baseline: 1.0207x; 1.0207x over previous
_Z11main_kernelPKfPKhS0_S0_Pf:
	s_ashr_i32 s38, s2, 2
	v_readfirstlane_b32 s3, v0
	s_and_b32 s37, s2, 7
	s_and_b32 s12, s38, 0xfffff8
	s_lshr_b32 s36, s3, 7
	s_or_b32 s12, s12, s37
	s_lshr_b32 s44, s12, 3
	s_lshl_b32 s44, s44, 1
	s_and_b32 s50, s12, 1
	s_or_b32 s44, s44, s50
	s_and_b32 s44, s44, 15
	s_lshl_b32 s48, s44, 15
	s_lshl_b32 s44, s44, 8
	s_add_i32 s46, s44, 0x100
	s_add_i32 s49, s44, 0x200
	s_bfe_u32 s31, s3, 0x10006
	s_lshl_b32 s12, s12, 8
	s_lshl_b32 s33, s36, 6
	s_load_dwordx8 s[4:11], s[0:1], 0x0
	s_add_i32 s28, s33, s12
	s_lshl_b32 s34, s31, 5
	s_or_b32 s12, s28, s34
	s_lshr_b32 s30, s3, 6
	s_lshl_b32 s39, s12, 12
	s_cmpk_gt_u32 s3, 0xff
	v_lshlrev_b32_e32 v2, 3, v0
	s_cselect_b64 s[24:25], -1, 0
	s_cmpk_lt_u32 s3, 0x100
	v_mov_b32_e32 v3, 0
	s_cselect_b64 s[26:27], -1, 0
	s_mov_b32 s14, 0x200000
	s_bfe_u32 s40, s2, 0x20003
	s_add_i32 s51, s39, s44
	s_and_b32 s52, s46, 0xf00
	s_add_i32 s52, s52, s39
	s_waitcnt lgkmcnt(0)
	s_mov_b32 s41, 0x201000
	s_load_dword s41, s[6:7], s41 offset:0x0
	v_lshl_add_u64 v[4:5], s[6:7], 0, v[2:3]
	v_add_co_u32_e32 v4, vcc, s14, v4
	s_lshl_b32 s29, s40, 8
	s_nop 0
	v_addc_co_u32_e32 v5, vcc, 0, v5, vcc
	v_or_b32_e32 v1, s29, v0
	v_add_lshl_u32 v6, s29, v0, 2
	v_mov_b32_e32 v7, v3
	s_movk_i32 s2, 0xfc00
	s_movk_i32 s12, 0x100
	global_load_dwordx2 v[8:9], v[4:5], off
	v_lshlrev_b32_e32 v4, 2, v1
	v_mov_b32_e32 v5, v3
	v_lshl_add_u64 v[6:7], s[8:9], 0, v[6:7]
	s_mov_b32 s3, -1
	v_lshl_add_u64 v[4:5], s[10:11], 0, v[4:5]
	v_lshl_add_u64 v[6:7], v[6:7], 0, s[2:3]
	v_cmp_gt_u32_e32 vcc, s12, v0
	s_load_dwordx2 s[8:9], s[0:1], 0x20
	v_bfe_u32 v1, v0, 3, 1
	v_cndmask_b32_e32 v5, v7, v5, vcc
	v_cndmask_b32_e32 v4, v6, v4, vcc
	global_load_dword v10, v[4:5], off
	v_lshl_or_b32 v1, s31, 2, v1
	v_and_b32_e32 v198, 15, v0
	v_bfe_u32 v199, v0, 4, 2
	v_mul_u32_u24_e32 v67, 0x440, v1
	v_lshrrev_b32_e32 v1, 1, v0
	v_lshlrev_b32_e32 v200, 4, v198
	v_bfe_u32 v4, v0, 1, 2
	v_bitop3_b32 v1, v199, v1, 3 bitop3:0x78
	s_mul_i32 s10, s36, 0x2200
	s_mov_b32 s15, 0x20000
	s_and_b32 s17, s5, 0xffff
	v_and_b32_e32 v66, 63, v0
	v_lshlrev_b32_e32 v68, 8, v4
	v_lshlrev_b32_e32 v69, 4, v1
	v_and_b32_e32 v70, 8, v2
	v_bitop3_b32 v71, v199, v0, 15 bitop3:0x78
	s_and_b32 s13, s7, 0xffff
	s_mov_b32 s12, s6
	s_mov_b32 s20, s6
	v_lshl_or_b32 v1, v199, 12, v200
	s_brev_b32 s18, 16
	s_mov_b32 s19, s15
	s_mov_b32 s16, s4
	s_mov_b32 s0, s4
	s_mov_b32 s1, s17
	s_add_i32 s10, s10, 0x10000
	s_mov_b32 s35, 0
	s_mov_b32 s21, s13
	s_mov_b32 s22, s14
	s_mov_b32 s23, s15
	s_mov_b32 s2, s18
	s_mov_b32 s3, s15
	s_or_b32 s4, s51, 0x4000
	buffer_load_dwordx4 v[4:7], v1, s[0:3], s51 offen nt sc1
	buffer_load_dwordx4 v[18:21], v1, s[0:3], s4 offen nt sc1
	s_or_b32 s4, s51, 0x8000
	s_or_b32 s5, s51, 0xc000
	buffer_load_dwordx4 v[22:25], v1, s[0:3], s4 offen nt sc1
	buffer_load_dwordx4 v[26:29], v1, s[0:3], s5 offen nt sc1
	s_or_b32 s4, s51, 0x10000
	s_or_b32 s5, s51, 0x14000
	buffer_load_dwordx4 v[34:37], v1, s[0:3], s4 offen nt sc1
	buffer_load_dwordx4 v[42:45], v1, s[0:3], s5 offen nt sc1
	s_or_b32 s4, s51, 0x18000
	s_or_b32 s5, s51, 0x1c000
	buffer_load_dwordx4 v[46:49], v1, s[0:3], s4 offen nt sc1
	buffer_load_dwordx4 v[58:61], v1, s[0:3], s5 offen nt sc1
	s_lshl_b32 s4, s30, 10
	v_lshlrev_b32_e32 v189, 4, v0
	s_lshl_b32 s5, s40, 19
	s_add_i32 s53, s5, s48
	s_mov_b32 m0, s4
	s_or_b32 s11, s53, 0x2000
	buffer_load_dwordx4 v189, s[20:23], s53 offen lds
	s_add_i32 m0, s4, 0x2000
	s_nop 0
	buffer_load_dwordx4 v189, s[20:23], s11 offen lds
	s_add_i32 m0, s4, 0x4000
	s_or_b32 s11, s53, 0x4000
	buffer_load_dwordx4 v189, s[20:23], s11 offen lds
	s_add_i32 m0, s4, 0x6000
	s_or_b32 s11, s53, 0x6000
	buffer_load_dwordx4 v189, s[20:23], s11 offen lds
	s_mov_b32 s20, 0x44800000
	s_waitcnt vmcnt(13)
	v_pk_mul_f32 v[8:9], v[8:9], s[20:21] op_sel_hi:[1,0]
	v_add_u32_e32 v2, 0x21000, v2
	ds_write_b64 v2, v[8:9]
	v_mov_b32_e32 v2, 0x22000
	v_lshl_add_u32 v2, v0, 2, v2
	s_waitcnt vmcnt(12)
	ds_write_b32 v2, v10
	s_waitcnt lgkmcnt(0)
	s_barrier
	s_or_b32 s11, s52, 0x0
	s_or_b32 s20, s52, 0x4000
	buffer_load_dwordx4 v[10:13], v1, s[0:3], s11 offen nt sc1
	buffer_load_dwordx4 v[14:17], v1, s[0:3], s20 offen nt sc1
	s_or_b32 s11, s52, 0x8000
	s_or_b32 s20, s52, 0xc000
	buffer_load_dwordx4 v[30:33], v1, s[0:3], s11 offen nt sc1
	buffer_load_dwordx4 v[38:41], v1, s[0:3], s20 offen nt sc1
	s_or_b32 s11, s52, 0x10000
	s_or_b32 s20, s52, 0x14000
	buffer_load_dwordx4 v[50:53], v1, s[0:3], s11 offen nt sc1
	buffer_load_dwordx4 v[54:57], v1, s[0:3], s20 offen nt sc1
	s_or_b32 s11, s52, 0x18000
	s_or_b32 s20, s52, 0x1c000
	buffer_load_dwordx4 v[74:77], v1, s[0:3], s11 offen nt sc1
	buffer_load_dwordx4 v[78:81], v1, s[0:3], s20 offen nt sc1
	v_or_b32_e32 v162, 0x21000, v200
	v_add_u32_e32 v249, s44, v162
	ds_read_b128 v[62:65], v249
	v_add3_u32 v9, s10, v67, v68
	v_or3_b32 v188, v9, v69, v70
	s_waitcnt vmcnt(19)
	v_cvt_pk_f16_f32 v7, v6, v7
	v_cvt_pk_f16_f32 v6, v4, v5
	s_waitcnt lgkmcnt(0)
	v_cvt_pk_f16_f32 v8, v62, v63
	v_mov_b32_e32 v185, v3
	s_waitcnt vmcnt(18)
	v_cvt_pk_f16_f32 v5, v20, v21
	v_cvt_pk_f16_f32 v4, v18, v19
	v_mov_b32_e32 v184, v3
	v_cvt_pk_f16_f32 v2, v64, v65
	v_dot2c_f32_f16_e32 v185, v6, v8
	v_dot2c_f32_f16_e32 v184, v4, v8
	ds_write2_b64 v188, v[6:7], v[4:5] offset1:8
	s_waitcnt vmcnt(17)
	v_cvt_pk_f16_f32 v4, v22, v23
	v_mov_b32_e32 v183, v3
	s_waitcnt vmcnt(16)
	v_cvt_pk_f16_f32 v6, v26, v27
	v_mov_b32_e32 v181, v3
	v_dot2c_f32_f16_e32 v185, v7, v2
	v_dot2c_f32_f16_e32 v184, v5, v2
	v_cvt_pk_f16_f32 v5, v24, v25
	v_dot2c_f32_f16_e32 v183, v4, v8
	v_cvt_pk_f16_f32 v7, v28, v29
	v_dot2c_f32_f16_e32 v181, v6, v8
	v_dot2c_f32_f16_e32 v183, v5, v2
	v_dot2c_f32_f16_e32 v181, v7, v2
	ds_write2_b64 v188, v[4:5], v[6:7] offset0:16 offset1:24
	s_waitcnt vmcnt(15)
	v_cvt_pk_f16_f32 v5, v36, v37
	v_cvt_pk_f16_f32 v4, v34, v35
	v_mov_b32_e32 v182, v3
	s_waitcnt vmcnt(14)
	v_cvt_pk_f16_f32 v7, v44, v45
	v_cvt_pk_f16_f32 v6, v42, v43
	v_mov_b32_e32 v178, v3
	v_add_u32_e32 v9, 0x800, v188
	v_dot2c_f32_f16_e32 v182, v4, v8
	v_dot2c_f32_f16_e32 v178, v6, v8
	ds_write2_b64 v9, v[4:5], v[6:7] offset0:16 offset1:24
	s_waitcnt vmcnt(13)
	v_cvt_pk_f16_f32 v4, v46, v47
	v_mov_b32_e32 v179, v3
	s_waitcnt vmcnt(12)
	v_cvt_pk_f16_f32 v6, v58, v59
	v_mov_b32_e32 v180, v3
	v_dot2c_f32_f16_e32 v182, v5, v2
	v_dot2c_f32_f16_e32 v178, v7, v2
	v_cvt_pk_f16_f32 v5, v48, v49
	v_dot2c_f32_f16_e32 v179, v4, v8
	v_cvt_pk_f16_f32 v7, v60, v61
	v_dot2c_f32_f16_e32 v180, v6, v8
	v_dot2c_f32_f16_e32 v179, v5, v2
	v_dot2c_f32_f16_e32 v180, v7, v2
	ds_write2_b64 v9, v[4:5], v[6:7] offset0:32 offset1:40
	s_waitcnt vmcnt(8) lgkmcnt(0)
	s_barrier
	s_lshl_b32 s0, s38, 20
	v_lshl_add_u32 v2, v199, 8, s10
	s_and_b32 s0, s0, 0xff800000
	s_lshl_b32 s1, s37, 20
	v_lshl_or_b32 v187, v71, 4, v2
	v_lshlrev_b32_e32 v2, 4, v66
	s_or_b32 s0, s0, s1
	s_lshl_b32 s1, s36, 18
	v_lshl_or_b32 v186, s31, 14, v2
	s_add_i32 s0, s0, s1
	s_lshl_b32 s1, s31, 17
	v_cndmask_b32_e64 v2, 0, 1, s[26:27]
	s_or_b32 s11, s0, s1
	v_or_b32_e32 v163, 0x21100, v200
	s_mov_b32 s10, -1
	v_cmp_ne_u32_e64 s[0:1], 1, v2
	s_mov_b32 s20, 0
	v_mov_b32_e32 v2, v3
	v_mov_b32_e32 v4, v3
	v_mov_b32_e32 v5, v3
	v_mov_b32_e32 v26, v3
	v_mov_b32_e32 v27, v3
	v_mov_b32_e32 v28, v3
	v_mov_b32_e32 v29, v3
	v_mov_b32_e32 v42, v3
	v_mov_b32_e32 v43, v3
	v_mov_b32_e32 v44, v3
	v_mov_b32_e32 v45, v3
	v_mov_b32_e32 v46, v3
	v_mov_b32_e32 v47, v3
	v_mov_b32_e32 v48, v3
	v_mov_b32_e32 v49, v3
	v_mov_b32_e32 v6, v3
	v_mov_b32_e32 v7, v3
	v_mov_b32_e32 v8, v3
	v_mov_b32_e32 v9, v3
	v_mov_b32_e32 v18, v3
	v_mov_b32_e32 v19, v3
	v_mov_b32_e32 v20, v3
	v_mov_b32_e32 v21, v3
	v_mov_b32_e32 v22, v3
	v_mov_b32_e32 v23, v3
	v_mov_b32_e32 v24, v3
	v_mov_b32_e32 v25, v3
	v_mov_b32_e32 v34, v3
	v_mov_b32_e32 v35, v3
	v_mov_b32_e32 v36, v3
	v_mov_b32_e32 v37, v3
	v_mov_b32_e32 v82, v3
	v_mov_b32_e32 v83, v3
	v_mov_b32_e32 v84, v3
	v_mov_b32_e32 v85, v3
	v_mov_b32_e32 v86, v3
	v_mov_b32_e32 v87, v3
	v_mov_b32_e32 v88, v3
	v_mov_b32_e32 v89, v3
	v_mov_b32_e32 v98, v3
	v_mov_b32_e32 v99, v3
	v_mov_b32_e32 v100, v3
	v_mov_b32_e32 v101, v3
	v_mov_b32_e32 v106, v3
	v_mov_b32_e32 v107, v3
	v_mov_b32_e32 v108, v3
	v_mov_b32_e32 v109, v3
	v_mov_b32_e32 v58, v3
	v_mov_b32_e32 v59, v3
	v_mov_b32_e32 v60, v3
	v_mov_b32_e32 v61, v3
	v_mov_b32_e32 v62, v3
	v_mov_b32_e32 v63, v3
	v_mov_b32_e32 v64, v3
	v_mov_b32_e32 v65, v3
	v_mov_b32_e32 v66, v3
	v_mov_b32_e32 v67, v3
	v_mov_b32_e32 v68, v3
	v_mov_b32_e32 v69, v3
	v_mov_b32_e32 v70, v3
	v_mov_b32_e32 v71, v3
	v_mov_b32_e32 v72, v3
	v_mov_b32_e32 v73, v3
	v_mov_b32_e32 v118, v3
	v_mov_b32_e32 v119, v3
	v_mov_b32_e32 v120, v3
	v_mov_b32_e32 v121, v3
	v_mov_b32_e32 v122, v3
	v_mov_b32_e32 v123, v3
	v_mov_b32_e32 v124, v3
	v_mov_b32_e32 v125, v3
	v_mov_b32_e32 v134, v3
	v_mov_b32_e32 v135, v3
	v_mov_b32_e32 v136, v3
	v_mov_b32_e32 v137, v3
	v_mov_b32_e32 v138, v3
	v_mov_b32_e32 v139, v3
	v_mov_b32_e32 v140, v3
	v_mov_b32_e32 v141, v3
	v_mov_b32_e32 v94, v3
	v_mov_b32_e32 v95, v3
	v_mov_b32_e32 v96, v3
	v_mov_b32_e32 v97, v3
	v_mov_b32_e32 v102, v3
	v_mov_b32_e32 v103, v3
	v_mov_b32_e32 v104, v3
	v_mov_b32_e32 v105, v3
	v_mov_b32_e32 v110, v3
	v_mov_b32_e32 v111, v3
	v_mov_b32_e32 v112, v3
	v_mov_b32_e32 v113, v3
	v_mov_b32_e32 v90, v3
	v_mov_b32_e32 v91, v3
	v_mov_b32_e32 v92, v3
	v_mov_b32_e32 v93, v3
	v_mov_b32_e32 v142, v3
	v_mov_b32_e32 v143, v3
	v_mov_b32_e32 v144, v3
	v_mov_b32_e32 v145, v3
	v_mov_b32_e32 v146, v3
	v_mov_b32_e32 v147, v3
	v_mov_b32_e32 v148, v3
	v_mov_b32_e32 v149, v3
	v_mov_b32_e32 v154, v3
	v_mov_b32_e32 v155, v3
	v_mov_b32_e32 v156, v3
	v_mov_b32_e32 v157, v3
	v_mov_b32_e32 v150, v3
	v_mov_b32_e32 v151, v3
	v_mov_b32_e32 v152, v3
	v_mov_b32_e32 v153, v3
	v_mov_b32_e32 v114, v3
	v_mov_b32_e32 v115, v3
	v_mov_b32_e32 v116, v3
	v_mov_b32_e32 v117, v3
	v_mov_b32_e32 v126, v3
	v_mov_b32_e32 v127, v3
	v_mov_b32_e32 v128, v3
	v_mov_b32_e32 v129, v3
	v_mov_b32_e32 v130, v3
	v_mov_b32_e32 v131, v3
	v_mov_b32_e32 v132, v3
	v_mov_b32_e32 v133, v3
	v_mov_b32_e32 v158, v3
	v_mov_b32_e32 v159, v3
	v_mov_b32_e32 v160, v3
	v_mov_b32_e32 v161, v3
	s_add_i32 s22, s10, 2
	s_add_i32 s54, s20, s46
	s_and_b32 s54, s54, 0xf00
	v_add_u32_e32 v164, s54, v162
.LBB1_2:
	s_bitcmp1_b32 s22, 0
	s_cselect_b32 s2, 0x8800, 0
	v_add_u32_e32 v244, s2, v188
	v_add_u32_e32 v245, 0x800, v244
	ds_read_b128 v[240:243], v164
	s_add_i32 s10, s10, 1
	s_and_b32 s2, s10, 1
	v_lshl_or_b32 v165, s2, 15, v186
	ds_read_b128 v[166:169], v165
	ds_read_b128 v[190:193], v165 offset:2048
	ds_read_b128 v[206:209], v165 offset:4096
	ds_read_b128 v[210:213], v165 offset:6144
	s_mul_i32 s3, s2, 0x8800
	v_add_u32_e32 v201, s3, v187
	ds_read_b128 v[170:173], v201
	ds_read_b128 v[174:177], v201 offset:2176
	ds_read_b128 v[194:197], v201 offset:4352
	ds_read_b128 v[202:205], v201 offset:6528
	s_add_i32 s21, s35, 0x8000
	s_and_b32 s2, s21, 0x8000
	s_add_i32 s2, s4, s2
	s_add_i32 s3, s21, s48
	s_and_b32 s3, s3, 0x78000
	s_add_i32 s3, s3, s5
	s_add_i32 s23, s3, 0
	s_mov_b32 m0, s2
	s_nop 0
	buffer_load_dwordx4 v189, s[12:15], s23 offen lds
	s_add_i32 m0, s2, 0x2000
	s_add_i32 s23, s3, 0x2000
	buffer_load_dwordx4 v189, s[12:15], s23 offen lds
	s_add_i32 m0, s2, 0x4000
	s_add_i32 s23, s3, 0x4000
	buffer_load_dwordx4 v189, s[12:15], s23 offen lds
	s_add_i32 m0, s2, 0x6000
	s_add_i32 s3, s3, 0x6000
	buffer_load_dwordx4 v189, s[12:15], s3 offen lds
	s_waitcnt lgkmcnt(8)
	v_cvt_pk_f16_f32 v238, v240, v241
	v_cvt_pk_f16_f32 v239, v242, v243
	s_add_i32 s2, s20, s49
	s_and_b32 s2, s2, 0xf00
	s_add_i32 s2, s2, s11
	s_waitcnt vmcnt(10)
	v_cvt_pk_f16_f32 v230, v10, v11
	v_cvt_pk_f16_f32 v231, v12, v13
	v_cvt_pk_f16_f32 v232, v14, v15
	v_cvt_pk_f16_f32 v233, v16, v17
	v_dot2c_f32_f16_e32 v185, v230, v238
	v_dot2c_f32_f16_e32 v184, v232, v238
	v_dot2c_f32_f16_e32 v185, v231, v239
	v_dot2c_f32_f16_e32 v184, v233, v239
	ds_write2_b64 v244, v[230:231], v[232:233] offset1:8
	s_add_i32 s3, s2, 0x0
	buffer_load_dwordx4 v[10:13], v1, s[16:19], s3 offen nt sc1
	s_add_i32 s3, s2, 0x4000
	buffer_load_dwordx4 v[14:17], v1, s[16:19], s3 offen nt sc1
	s_waitcnt lgkmcnt(3)
	v_mfma_f32_16x16x32_f16 v[106:109], v[166:169], v[170:173], v[106:109]
	v_mfma_f32_16x16x32_f16 v[98:101], v[190:193], v[170:173], v[98:101]
	v_mfma_f32_16x16x32_f16 v[86:89], v[206:209], v[170:173], v[86:89]
	s_waitcnt vmcnt(10)
	v_cvt_pk_f16_f32 v234, v30, v31
	ds_read_b128 v[214:217], v165 offset:8192
	v_mfma_f32_16x16x32_f16 v[82:85], v[210:213], v[170:173], v[82:85]
	v_cvt_pk_f16_f32 v235, v32, v33
	s_waitcnt lgkmcnt(3)
	v_mfma_f32_16x16x32_f16 v[46:49], v[166:169], v[174:177], v[46:49]
	v_cvt_pk_f16_f32 v236, v38, v39
	v_mfma_f32_16x16x32_f16 v[42:45], v[190:193], v[174:177], v[42:45]
	v_cvt_pk_f16_f32 v237, v40, v41
	ds_read_b128 v[218:221], v165 offset:10240
	v_mfma_f32_16x16x32_f16 v[26:29], v[206:209], v[174:177], v[26:29]
	v_dot2c_f32_f16_e32 v183, v234, v238
	v_mfma_f32_16x16x32_f16 v[2:5], v[210:213], v[174:177], v[2:5]
	v_dot2c_f32_f16_e32 v181, v236, v238
	s_waitcnt lgkmcnt(3)
	v_mfma_f32_16x16x32_f16 v[118:121], v[166:169], v[194:197], v[118:121]
	v_dot2c_f32_f16_e32 v183, v235, v239
	ds_read_b128 v[222:225], v165 offset:12288
	v_mfma_f32_16x16x32_f16 v[122:125], v[190:193], v[194:197], v[122:125]
	v_dot2c_f32_f16_e32 v181, v237, v239
	v_mfma_f32_16x16x32_f16 v[134:137], v[206:209], v[194:197], v[134:137]
	ds_write2_b64 v244, v[234:235], v[236:237] offset0:16 offset1:24
	v_mfma_f32_16x16x32_f16 v[138:141], v[210:213], v[194:197], v[138:141]
	s_add_i32 s3, s2, 0x8000
	buffer_load_dwordx4 v[30:33], v1, s[16:19], s3 offen nt sc1
	ds_read_b128 v[226:229], v165 offset:14336
	s_waitcnt lgkmcnt(4)
	v_mfma_f32_16x16x32_f16 v[142:145], v[166:169], v[202:205], v[142:145]
	s_add_i32 s3, s2, 0xc000
	buffer_load_dwordx4 v[38:41], v1, s[16:19], s3 offen nt sc1
	v_mfma_f32_16x16x32_f16 v[146:149], v[190:193], v[202:205], v[146:149]
	s_waitcnt vmcnt(10)
	v_cvt_pk_f16_f32 v230, v50, v51
	v_mfma_f32_16x16x32_f16 v[154:157], v[206:209], v[202:205], v[154:157]
	v_cvt_pk_f16_f32 v231, v52, v53
	ds_read_b128 v[166:169], v165 offset:1024
	v_mfma_f32_16x16x32_f16 v[150:153], v[210:213], v[202:205], v[150:153]
	v_cvt_pk_f16_f32 v232, v54, v55
	s_waitcnt lgkmcnt(4)
	v_mfma_f32_16x16x32_f16 v[34:37], v[214:217], v[170:173], v[34:37]
	v_cvt_pk_f16_f32 v233, v56, v57
	s_waitcnt lgkmcnt(3)
	v_mfma_f32_16x16x32_f16 v[22:25], v[218:221], v[170:173], v[22:25]
	v_dot2c_f32_f16_e32 v182, v230, v238
	ds_read_b128 v[190:193], v165 offset:3072
	s_waitcnt lgkmcnt(3)
	v_mfma_f32_16x16x32_f16 v[18:21], v[222:225], v[170:173], v[18:21]
	v_dot2c_f32_f16_e32 v178, v232, v238
	s_waitcnt lgkmcnt(2)
	v_mfma_f32_16x16x32_f16 v[6:9], v[226:229], v[170:173], v[6:9]
	v_dot2c_f32_f16_e32 v182, v231, v239
	v_mfma_f32_16x16x32_f16 v[58:61], v[214:217], v[174:177], v[58:61]
	v_dot2c_f32_f16_e32 v178, v233, v239
	ds_read_b128 v[170:173], v165 offset:5120
	v_mfma_f32_16x16x32_f16 v[62:65], v[218:221], v[174:177], v[62:65]
	ds_write2_b64 v245, v[230:231], v[232:233] offset0:16 offset1:24
	v_mfma_f32_16x16x32_f16 v[66:69], v[222:225], v[174:177], v[66:69]
	s_add_i32 s3, s2, 0x10000
	buffer_load_dwordx4 v[50:53], v1, s[16:19], s3 offen nt sc1
	v_mfma_f32_16x16x32_f16 v[70:73], v[226:229], v[174:177], v[70:73]
	s_add_i32 s3, s2, 0x14000
	buffer_load_dwordx4 v[54:57], v1, s[16:19], s3 offen nt sc1
	ds_read_b128 v[174:177], v165 offset:7168
	v_mfma_f32_16x16x32_f16 v[94:97], v[214:217], v[194:197], v[94:97]
	s_waitcnt vmcnt(10)
	v_cvt_pk_f16_f32 v234, v74, v75
	v_mfma_f32_16x16x32_f16 v[102:105], v[218:221], v[194:197], v[102:105]
	v_cvt_pk_f16_f32 v235, v76, v77
	v_mfma_f32_16x16x32_f16 v[110:113], v[222:225], v[194:197], v[110:113]
	v_cvt_pk_f16_f32 v236, v78, v79
	ds_read_b128 v[206:209], v201 offset:1088
	v_mfma_f32_16x16x32_f16 v[90:93], v[226:229], v[194:197], v[90:93]
	v_cvt_pk_f16_f32 v237, v80, v81
	v_mfma_f32_16x16x32_f16 v[114:117], v[214:217], v[202:205], v[114:117]
	v_dot2c_f32_f16_e32 v179, v234, v238
	v_mfma_f32_16x16x32_f16 v[126:129], v[218:221], v[202:205], v[126:129]
	v_dot2c_f32_f16_e32 v180, v236, v238
	ds_read_b128 v[194:197], v201 offset:3264
	v_mfma_f32_16x16x32_f16 v[130:133], v[222:225], v[202:205], v[130:133]
	v_dot2c_f32_f16_e32 v179, v235, v239
	v_mfma_f32_16x16x32_f16 v[158:161], v[226:229], v[202:205], v[158:161]
	v_dot2c_f32_f16_e32 v180, v237, v239
	s_waitcnt lgkmcnt(1)
	v_mfma_f32_16x16x32_f16 v[106:109], v[166:169], v[206:209], v[106:109]
	ds_write2_b64 v245, v[234:235], v[236:237] offset0:32 offset1:40
	ds_read_b128 v[202:205], v201 offset:5440
	v_mfma_f32_16x16x32_f16 v[98:101], v[190:193], v[206:209], v[98:101]
	s_add_i32 s3, s2, 0x18000
	buffer_load_dwordx4 v[74:77], v1, s[16:19], s3 offen nt sc1
	v_mfma_f32_16x16x32_f16 v[86:89], v[170:173], v[206:209], v[86:89]
	s_add_i32 s3, s2, 0x1c000
	buffer_load_dwordx4 v[78:81], v1, s[16:19], s3 offen nt sc1
	v_mfma_f32_16x16x32_f16 v[82:85], v[174:177], v[206:209], v[82:85]
	ds_read_b128 v[210:213], v201 offset:7616
	s_waitcnt lgkmcnt(2)
	v_mfma_f32_16x16x32_f16 v[46:49], v[166:169], v[194:197], v[46:49]
	v_mfma_f32_16x16x32_f16 v[42:45], v[190:193], v[194:197], v[42:45]
	v_mfma_f32_16x16x32_f16 v[26:29], v[170:173], v[194:197], v[26:29]
	ds_read_b128 v[214:217], v165 offset:9216
	v_mfma_f32_16x16x32_f16 v[2:5], v[174:177], v[194:197], v[2:5]
	s_waitcnt lgkmcnt(2)
	v_mfma_f32_16x16x32_f16 v[118:121], v[166:169], v[202:205], v[118:121]
	v_mfma_f32_16x16x32_f16 v[122:125], v[190:193], v[202:205], v[122:125]
	ds_read_b128 v[218:221], v165 offset:11264
	v_mfma_f32_16x16x32_f16 v[134:137], v[170:173], v[202:205], v[134:137]
	v_mfma_f32_16x16x32_f16 v[138:141], v[174:177], v[202:205], v[138:141]
	s_waitcnt lgkmcnt(2)
	v_mfma_f32_16x16x32_f16 v[142:145], v[166:169], v[210:213], v[142:145]
	ds_read_b128 v[166:169], v165 offset:13312
	v_mfma_f32_16x16x32_f16 v[146:149], v[190:193], v[210:213], v[146:149]
	v_mfma_f32_16x16x32_f16 v[154:157], v[170:173], v[210:213], v[154:157]
	v_mfma_f32_16x16x32_f16 v[150:153], v[174:177], v[210:213], v[150:153]
	ds_read_b128 v[170:173], v165 offset:15360
	s_waitcnt lgkmcnt(3)
	v_mfma_f32_16x16x32_f16 v[34:37], v[214:217], v[206:209], v[34:37]
	s_waitcnt lgkmcnt(2)
	v_mfma_f32_16x16x32_f16 v[22:25], v[218:221], v[206:209], v[22:25]
	s_waitcnt lgkmcnt(1)
	v_mfma_f32_16x16x32_f16 v[18:21], v[166:169], v[206:209], v[18:21]
	s_waitcnt lgkmcnt(0)
	v_mfma_f32_16x16x32_f16 v[6:9], v[170:173], v[206:209], v[6:9]
	v_mfma_f32_16x16x32_f16 v[58:61], v[214:217], v[194:197], v[58:61]
	v_mfma_f32_16x16x32_f16 v[62:65], v[218:221], v[194:197], v[62:65]
	v_mfma_f32_16x16x32_f16 v[66:69], v[166:169], v[194:197], v[66:69]
	v_mfma_f32_16x16x32_f16 v[70:73], v[170:173], v[194:197], v[70:73]
	v_mfma_f32_16x16x32_f16 v[94:97], v[214:217], v[202:205], v[94:97]
	v_mfma_f32_16x16x32_f16 v[102:105], v[218:221], v[202:205], v[102:105]
	v_mfma_f32_16x16x32_f16 v[110:113], v[166:169], v[202:205], v[110:113]
	v_mfma_f32_16x16x32_f16 v[90:93], v[170:173], v[202:205], v[90:93]
	v_mfma_f32_16x16x32_f16 v[114:117], v[214:217], v[210:213], v[114:117]
	v_mfma_f32_16x16x32_f16 v[126:129], v[218:221], v[210:213], v[126:129]
	v_mfma_f32_16x16x32_f16 v[130:133], v[166:169], v[210:213], v[130:133]
	v_mfma_f32_16x16x32_f16 v[158:161], v[170:173], v[210:213], v[158:161]
	s_waitcnt vmcnt(8) lgkmcnt(0)
	s_barrier
	s_addk_i32 s20, 0x100
	s_cmpk_eq_i32 s20, 0xe00
	s_cbranch_scc1 .Lmy_exit
	s_mov_b32 s35, s21
	s_add_i32 s22, s10, 2
	s_add_i32 s54, s20, s46
	s_and_b32 s54, s54, 0xf00
	v_add_u32_e32 v164, s54, v162
	s_branch .LBB1_2

.LBB1_10:
	s_add_i32 s11, s10, 2
	s_and_b64 vcc, exec, s[0:1]
	s_lshl_b32 s54, s11, 8
	s_add_i32 s54, s54, s44
	s_and_b32 s54, s54, 0xf00
	v_add_u32_e32 v190, s54, v162
	s_waitcnt vmcnt(7)
	v_cvt_pk_f16_f32 v175, v12, v13
	v_cvt_pk_f16_f32 v174, v10, v11
	s_waitcnt vmcnt(6)
	v_cvt_pk_f16_f32 v177, v16, v17
	v_cvt_pk_f16_f32 v176, v14, v15
	s_waitcnt vmcnt(5)
	v_cvt_pk_f16_f32 v171, v32, v33
	v_cvt_pk_f16_f32 v170, v30, v31
	s_waitcnt vmcnt(4)
	v_cvt_pk_f16_f32 v173, v40, v41
	v_cvt_pk_f16_f32 v172, v38, v39
	s_waitcnt vmcnt(3)
	v_cvt_pk_f16_f32 v167, v52, v53
	v_cvt_pk_f16_f32 v166, v50, v51
	s_waitcnt vmcnt(2)
	v_cvt_pk_f16_f32 v169, v56, v57
	v_cvt_pk_f16_f32 v168, v54, v55
	s_waitcnt vmcnt(1)
	v_cvt_pk_f16_f32 v163, v76, v77
	v_cvt_pk_f16_f32 v162, v74, v75
	s_waitcnt vmcnt(0)
	v_cvt_pk_f16_f32 v165, v80, v81
	v_cvt_pk_f16_f32 v164, v78, v79
	s_cbranch_vccnz .LBB1_12
	ds_read_b128 v[10:13], v190
	s_bitcmp1_b32 s10, 0
	s_cselect_b32 s0, 0x8800, 0
	v_add_u32_e32 v14, s0, v188
	ds_write2_b64 v14, v[174:175], v[176:177] offset1:8
	s_waitcnt lgkmcnt(1)
	v_cvt_pk_f16_f32 v10, v10, v11
	v_cvt_pk_f16_f32 v12, v12, v13
	v_dot2c_f32_f16_e32 v185, v174, v10
	v_dot2c_f32_f16_e32 v184, v176, v10
	v_dot2c_f32_f16_e32 v183, v170, v10
	v_dot2c_f32_f16_e32 v181, v172, v10
	v_dot2c_f32_f16_e32 v182, v166, v10
	v_dot2c_f32_f16_e32 v178, v168, v10
	v_dot2c_f32_f16_e32 v179, v162, v10
	v_dot2c_f32_f16_e32 v180, v164, v10
	v_dot2c_f32_f16_e32 v185, v175, v12
	v_dot2c_f32_f16_e32 v184, v177, v12
	v_dot2c_f32_f16_e32 v183, v171, v12
	v_dot2c_f32_f16_e32 v181, v173, v12
	v_dot2c_f32_f16_e32 v182, v167, v12
	v_dot2c_f32_f16_e32 v178, v169, v12
	v_add_u32_e32 v11, 0x800, v14
	v_dot2c_f32_f16_e32 v179, v163, v12
	v_dot2c_f32_f16_e32 v180, v165, v12
	ds_write2_b64 v14, v[170:171], v[172:173] offset0:16 offset1:24
	ds_write2_b64 v11, v[166:167], v[168:169] offset0:16 offset1:24
	ds_write2_b64 v11, v[162:163], v[164:165] offset0:32 offset1:40
.LBB1_12:
	s_lshl_b32 s0, s11, 15
	s_and_b32 s1, s0, 0x8000
	s_add_i32 s0, s0, s48
	s_and_b32 s0, s0, 0x78000
	s_add_i32 s1, s4, s1
	s_add_i32 s0, s0, s5
	s_mov_b32 m0, s1
	s_or_b32 s4, s0, 0x2000
	buffer_load_dwordx4 v189, s[12:15], s0 offen lds
	s_add_i32 m0, s1, 0x2000
	s_nop 0
	buffer_load_dwordx4 v189, s[12:15], s4 offen lds
	s_add_i32 m0, s1, 0x4000
	s_or_b32 s4, s0, 0x4000
	buffer_load_dwordx4 v189, s[12:15], s4 offen lds
	s_add_i32 m0, s1, 0x6000
	s_or_b32 s0, s0, 0x6000
	buffer_load_dwordx4 v189, s[12:15], s0 offen lds
	ds_read_b128 v[10:13], v186
	ds_read_b128 v[38:41], v186 offset:2048
	ds_read_b128 v[74:77], v186 offset:4096
	ds_read_b128 v[78:81], v186 offset:6144
	ds_read_b128 v[14:17], v187
	ds_read_b128 v[30:33], v187 offset:2176
	ds_read_b128 v[50:53], v187 offset:4352
	ds_read_b128 v[54:57], v187 offset:6528
	s_waitcnt lgkmcnt(3)
	v_mfma_f32_16x16x32_f16 v[106:109], v[10:13], v[14:17], v[106:109]
	v_mfma_f32_16x16x32_f16 v[98:101], v[38:41], v[14:17], v[98:101]
	v_mfma_f32_16x16x32_f16 v[192:195], v[74:77], v[14:17], v[86:89]
	s_nop 2
	ds_read_b128 v[86:89], v186 offset:8192
	v_mfma_f32_16x16x32_f16 v[82:85], v[78:81], v[14:17], v[82:85]
	s_waitcnt lgkmcnt(3)
	v_mfma_f32_16x16x32_f16 v[46:49], v[10:13], v[30:33], v[46:49]
	v_mfma_f32_16x16x32_f16 v[42:45], v[38:41], v[30:33], v[42:45]
	ds_read_b128 v[202:205], v186 offset:10240
	v_mfma_f32_16x16x32_f16 v[26:29], v[74:77], v[30:33], v[26:29]
	v_mfma_f32_16x16x32_f16 v[2:5], v[78:81], v[30:33], v[2:5]
	s_waitcnt lgkmcnt(3)
	v_mfma_f32_16x16x32_f16 v[118:121], v[10:13], v[50:53], v[118:121]
	ds_read_b128 v[206:209], v186 offset:12288
	v_mfma_f32_16x16x32_f16 v[122:125], v[38:41], v[50:53], v[122:125]
	v_mfma_f32_16x16x32_f16 v[134:137], v[74:77], v[50:53], v[134:137]
	v_mfma_f32_16x16x32_f16 v[138:141], v[78:81], v[50:53], v[138:141]
	ds_read_b128 v[210:213], v186 offset:14336
	s_waitcnt lgkmcnt(4)
	v_mfma_f32_16x16x32_f16 v[10:13], v[10:13], v[54:57], v[142:145]
	v_mfma_f32_16x16x32_f16 v[38:41], v[38:41], v[54:57], v[146:149]
	v_mfma_f32_16x16x32_f16 v[142:145], v[74:77], v[54:57], v[154:157]
	s_nop 1
	ds_read_b128 v[146:149], v186 offset:1024
	v_mfma_f32_16x16x32_f16 v[150:153], v[78:81], v[54:57], v[150:153]
	s_waitcnt lgkmcnt(4)
	v_mfma_f32_16x16x32_f16 v[34:37], v[86:89], v[14:17], v[34:37]
	s_waitcnt lgkmcnt(3)
	v_mfma_f32_16x16x32_f16 v[22:25], v[202:205], v[14:17], v[22:25]
	ds_read_b128 v[154:157], v186 offset:3072
	s_waitcnt lgkmcnt(3)
	v_mfma_f32_16x16x32_f16 v[18:21], v[206:209], v[14:17], v[18:21]
	s_waitcnt lgkmcnt(2)
	v_mfma_f32_16x16x32_f16 v[6:9], v[210:213], v[14:17], v[6:9]
	v_mfma_f32_16x16x32_f16 v[14:17], v[86:89], v[30:33], v[58:61]
	s_nop 2
	ds_read_b128 v[58:61], v186 offset:5120
	v_mfma_f32_16x16x32_f16 v[214:217], v[202:205], v[30:33], v[62:65]
	v_mfma_f32_16x16x32_f16 v[218:221], v[206:209], v[30:33], v[66:69]
	v_mfma_f32_16x16x32_f16 v[222:225], v[210:213], v[30:33], v[70:73]
	ds_read_b128 v[30:33], v186 offset:7168
	v_mfma_f32_16x16x32_f16 v[226:229], v[86:89], v[50:53], v[94:97]
	v_mfma_f32_16x16x32_f16 v[230:233], v[202:205], v[50:53], v[102:105]
	v_mfma_f32_16x16x32_f16 v[234:237], v[206:209], v[50:53], v[110:113]
	ds_read_b128 v[238:241], v187 offset:1088
	v_mfma_f32_16x16x32_f16 v[242:245], v[210:213], v[50:53], v[90:93]
	v_mfma_f32_16x16x32_f16 v[246:249], v[86:89], v[54:57], v[114:117]
	v_mfma_f32_16x16x32_f16 v[126:129], v[202:205], v[54:57], v[126:129]
	ds_read_b128 v[202:205], v187 offset:3264
	v_mfma_f32_16x16x32_f16 v[130:133], v[206:209], v[54:57], v[130:133]
	v_mfma_f32_16x16x32_f16 v[158:161], v[210:213], v[54:57], v[158:161]
	s_waitcnt lgkmcnt(1)
	v_mfma_f32_16x16x32_f16 v[66:69], v[146:149], v[238:241], v[106:109]
	ds_read_b128 v[206:209], v187 offset:5440
	v_mfma_f32_16x16x32_f16 v[86:89], v[154:157], v[238:241], v[98:101]
	v_mfma_f32_16x16x32_f16 v[90:93], v[58:61], v[238:241], v[192:195]
	v_mfma_f32_16x16x32_f16 v[70:73], v[30:33], v[238:241], v[82:85]
	s_nop 1
	ds_read_b128 v[192:195], v187 offset:7616
	s_waitcnt lgkmcnt(2)
	v_mfma_f32_16x16x32_f16 v[94:97], v[146:149], v[202:205], v[46:49]
	v_mfma_f32_16x16x32_f16 v[98:101], v[154:157], v[202:205], v[42:45]
	v_mfma_f32_16x16x32_f16 v[74:77], v[58:61], v[202:205], v[26:29]
	ds_read_b128 v[210:213], v186 offset:9216
	v_mfma_f32_16x16x32_f16 v[102:105], v[30:33], v[202:205], v[2:5]
	s_waitcnt lgkmcnt(2)
	v_mfma_f32_16x16x32_f16 v[106:109], v[146:149], v[206:209], v[118:121]
	v_mfma_f32_16x16x32_f16 v[78:81], v[154:157], v[206:209], v[122:125]
	ds_read_b128 v[2:5], v186 offset:11264
	v_mfma_f32_16x16x32_f16 v[110:113], v[58:61], v[206:209], v[134:137]
	v_mfma_f32_16x16x32_f16 v[114:117], v[30:33], v[206:209], v[138:141]
	s_waitcnt lgkmcnt(2)
	v_mfma_f32_16x16x32_f16 v[82:85], v[146:149], v[192:195], v[10:13]
	ds_read_b128 v[134:137], v186 offset:13312
	v_mfma_f32_16x16x32_f16 v[118:121], v[154:157], v[192:195], v[38:41]
	v_mfma_f32_16x16x32_f16 v[122:125], v[58:61], v[192:195], v[142:145]
	v_mfma_f32_16x16x32_f16 v[62:65], v[30:33], v[192:195], v[150:153]
	ds_read_b128 v[138:141], v186 offset:15360
	s_waitcnt lgkmcnt(3)
	v_mfma_f32_16x16x32_f16 v[54:57], v[210:213], v[238:241], v[34:37]
	s_waitcnt lgkmcnt(2)
	v_mfma_f32_16x16x32_f16 v[58:61], v[2:5], v[238:241], v[22:25]
	s_waitcnt lgkmcnt(1)
	v_mfma_f32_16x16x32_f16 v[42:45], v[134:137], v[238:241], v[18:21]
	s_waitcnt lgkmcnt(0)
	v_mfma_f32_16x16x32_f16 v[46:49], v[138:141], v[238:241], v[6:9]
	v_mfma_f32_16x16x32_f16 v[50:53], v[210:213], v[202:205], v[14:17]
	v_mfma_f32_16x16x32_f16 v[30:33], v[2:5], v[202:205], v[214:217]
	v_mfma_f32_16x16x32_f16 v[34:37], v[134:137], v[202:205], v[218:221]
	v_mfma_f32_16x16x32_f16 v[38:41], v[138:141], v[202:205], v[222:225]
	v_mfma_f32_16x16x32_f16 v[18:21], v[210:213], v[206:209], v[226:229]
	v_mfma_f32_16x16x32_f16 v[22:25], v[2:5], v[206:209], v[230:233]
	v_mfma_f32_16x16x32_f16 v[26:29], v[134:137], v[206:209], v[234:237]
	v_mfma_f32_16x16x32_f16 v[6:9], v[138:141], v[206:209], v[242:245]
	v_mfma_f32_16x16x32_f16 v[10:13], v[210:213], v[192:195], v[246:249]
	v_mfma_f32_16x16x32_f16 v[14:17], v[2:5], v[192:195], v[126:129]
	v_mfma_f32_16x16x32_f16 v[2:5], v[134:137], v[192:195], v[130:133]
	v_mfma_f32_16x16x32_f16 v[126:129], v[138:141], v[192:195], v[158:161]
	s_and_b64 vcc, exec, s[2:3]
	s_cbranch_vccnz .LBB1_14
	ds_read_b128 v[130:133], v190
	s_bitcmp1_b32 s10, 0
	s_cselect_b32 s0, 0x8800, 0
	v_add_u32_e32 v134, s0, v188
	ds_write2_b64 v134, v[174:175], v[176:177] offset1:8
	s_waitcnt lgkmcnt(1)
	v_cvt_pk_f16_f32 v130, v130, v131
	v_cvt_pk_f16_f32 v132, v132, v133
	v_dot2c_f32_f16_e32 v185, v174, v130
	v_dot2c_f32_f16_e32 v184, v176, v130
	v_dot2c_f32_f16_e32 v183, v170, v130
	v_dot2c_f32_f16_e32 v181, v172, v130
	v_dot2c_f32_f16_e32 v182, v166, v130
	v_dot2c_f32_f16_e32 v178, v168, v130
	v_dot2c_f32_f16_e32 v179, v162, v130
	v_dot2c_f32_f16_e32 v180, v164, v130
	v_dot2c_f32_f16_e32 v185, v175, v132
	v_dot2c_f32_f16_e32 v184, v177, v132
	v_dot2c_f32_f16_e32 v183, v171, v132
	v_dot2c_f32_f16_e32 v181, v173, v132
	v_dot2c_f32_f16_e32 v182, v167, v132
	v_dot2c_f32_f16_e32 v178, v169, v132
	v_add_u32_e32 v131, 0x800, v134
	v_dot2c_f32_f16_e32 v179, v163, v132
	v_dot2c_f32_f16_e32 v180, v165, v132
	ds_write2_b64 v134, v[170:171], v[172:173] offset0:16 offset1:24
	ds_write2_b64 v131, v[166:167], v[168:169] offset0:16 offset1:24
	ds_write2_b64 v131, v[162:163], v[164:165] offset0:32 offset1:40
.LBB1_14:
	v_add_f32_dpp v185, v185, v185 quad_perm:[1,0,3,2] row_mask:0xf bank_mask:0xf
	v_add_f32_dpp v184, v184, v184 quad_perm:[1,0,3,2] row_mask:0xf bank_mask:0xf
	v_add_f32_dpp v183, v183, v183 quad_perm:[1,0,3,2] row_mask:0xf bank_mask:0xf
	v_add_f32_dpp v181, v181, v181 quad_perm:[1,0,3,2] row_mask:0xf bank_mask:0xf
	v_add_f32_dpp v182, v182, v182 quad_perm:[1,0,3,2] row_mask:0xf bank_mask:0xf
	v_add_f32_dpp v178, v178, v178 quad_perm:[1,0,3,2] row_mask:0xf bank_mask:0xf
	v_add_f32_dpp v179, v179, v179 quad_perm:[1,0,3,2] row_mask:0xf bank_mask:0xf
	v_add_f32_dpp v180, v180, v180 quad_perm:[1,0,3,2] row_mask:0xf bank_mask:0xf
	v_add_f32_dpp v185, v185, v185 quad_perm:[2,3,0,1] row_mask:0xf bank_mask:0xf
	v_add_f32_dpp v184, v184, v184 quad_perm:[2,3,0,1] row_mask:0xf bank_mask:0xf
	v_add_f32_dpp v183, v183, v183 quad_perm:[2,3,0,1] row_mask:0xf bank_mask:0xf
	v_add_f32_dpp v181, v181, v181 quad_perm:[2,3,0,1] row_mask:0xf bank_mask:0xf
	v_add_f32_dpp v182, v182, v182 quad_perm:[2,3,0,1] row_mask:0xf bank_mask:0xf
	v_add_f32_dpp v178, v178, v178 quad_perm:[2,3,0,1] row_mask:0xf bank_mask:0xf
	v_add_f32_dpp v179, v179, v179 quad_perm:[2,3,0,1] row_mask:0xf bank_mask:0xf
	v_add_f32_dpp v180, v180, v180 quad_perm:[2,3,0,1] row_mask:0xf bank_mask:0xf
	v_add_f32_dpp v185, v185, v185 row_half_mirror row_mask:0xf bank_mask:0xf
	v_add_f32_dpp v184, v184, v184 row_half_mirror row_mask:0xf bank_mask:0xf
	v_add_f32_dpp v183, v183, v183 row_half_mirror row_mask:0xf bank_mask:0xf
	v_add_f32_dpp v181, v181, v181 row_half_mirror row_mask:0xf bank_mask:0xf
	v_add_f32_dpp v182, v182, v182 row_half_mirror row_mask:0xf bank_mask:0xf
	v_add_f32_dpp v178, v178, v178 row_half_mirror row_mask:0xf bank_mask:0xf
	v_add_f32_dpp v179, v179, v179 row_half_mirror row_mask:0xf bank_mask:0xf
	v_add_f32_dpp v180, v180, v180 row_half_mirror row_mask:0xf bank_mask:0xf
	v_add_f32_dpp v185, v185, v185 row_mirror row_mask:0xf bank_mask:0xf
	v_add_f32_dpp v184, v184, v184 row_mirror row_mask:0xf bank_mask:0xf
	v_add_f32_dpp v183, v183, v183 row_mirror row_mask:0xf bank_mask:0xf
	v_add_f32_dpp v181, v181, v181 row_mirror row_mask:0xf bank_mask:0xf
	v_add_f32_dpp v182, v182, v182 row_mirror row_mask:0xf bank_mask:0xf
	v_add_f32_dpp v178, v178, v178 row_mirror row_mask:0xf bank_mask:0xf
	v_add_f32_dpp v179, v179, v179 row_mirror row_mask:0xf bank_mask:0xf
	v_add_f32_dpp v180, v180, v180 row_mirror row_mask:0xf bank_mask:0xf
	v_cmp_eq_u32_e32 vcc, 0, v198
	s_and_saveexec_b64 s[0:1], vcc
	s_cbranch_execz .Lmy_bm_skip
	s_lshl_b32 s2, s34, 2
	s_lshl_b32 s3, s33, 2
	s_add_i32 s2, s2, s3
	v_lshl_add_u32 v130, v199, 2, s2
	v_add_u32_e32 v130, 0x22800, v130
	v_mov_b32_e32 v131, s41
	v_fmamk_f32 v132, v185, 0x3a800000, v131
	v_fmamk_f32 v133, v184, 0x3a800000, v131
	ds_write2_b32 v130, v132, v133 offset1:4
	v_fmamk_f32 v134, v183, 0x3a800000, v131
	v_fmamk_f32 v135, v181, 0x3a800000, v131
	ds_write2_b32 v130, v134, v135 offset0:8 offset1:12
	v_fmamk_f32 v136, v182, 0x3a800000, v131
	v_fmamk_f32 v137, v178, 0x3a800000, v131
	ds_write2_b32 v130, v136, v137 offset0:16 offset1:20
	v_fmamk_f32 v138, v179, 0x3a800000, v131
	v_fmamk_f32 v139, v180, 0x3a800000, v131
	ds_write2_b32 v130, v138, v139 offset0:24 offset1:28
.Lmy_bm_skip:
	s_or_b64 exec, exec, s[0:1]
	s_waitcnt vmcnt(0) lgkmcnt(0)
	s_barrier
	ds_read_b128 v[130:133], v186 offset:32768
	ds_read_b128 v[142:145], v186 offset:34816
	ds_read_b128 v[154:157], v186 offset:36864
	ds_read_b128 v[158:161], v186 offset:38912
	ds_read_b128 v[134:137], v187 offset:34816
	ds_read_b128 v[138:141], v187 offset:36992
	ds_read_b128 v[146:149], v187 offset:39168
	ds_read_b128 v[150:153], v187 offset:41344
	s_waitcnt lgkmcnt(3)
	v_mfma_f32_16x16x32_f16 v[66:69], v[130:133], v[134:137], v[66:69]
	v_mfma_f32_16x16x32_f16 v[86:89], v[142:145], v[134:137], v[86:89]
	v_mfma_f32_16x16x32_f16 v[90:93], v[154:157], v[134:137], v[90:93]
	ds_read_b128 v[162:165], v186 offset:40960
	v_mfma_f32_16x16x32_f16 v[70:73], v[158:161], v[134:137], v[70:73]
	s_waitcnt lgkmcnt(3)
	v_mfma_f32_16x16x32_f16 v[94:97], v[130:133], v[138:141], v[94:97]
	v_mfma_f32_16x16x32_f16 v[98:101], v[142:145], v[138:141], v[98:101]
	ds_read_b128 v[166:169], v186 offset:43008
	v_mfma_f32_16x16x32_f16 v[74:77], v[154:157], v[138:141], v[74:77]
	v_mfma_f32_16x16x32_f16 v[102:105], v[158:161], v[138:141], v[102:105]
	s_waitcnt lgkmcnt(3)
	v_mfma_f32_16x16x32_f16 v[106:109], v[130:133], v[146:149], v[106:109]
	ds_read_b128 v[170:173], v186 offset:45056
	v_mfma_f32_16x16x32_f16 v[78:81], v[142:145], v[146:149], v[78:81]
	v_mfma_f32_16x16x32_f16 v[110:113], v[154:157], v[146:149], v[110:113]
	v_mfma_f32_16x16x32_f16 v[174:177], v[158:161], v[146:149], v[114:117]
	s_nop 2
	ds_read_b128 v[114:117], v186 offset:47104
	s_waitcnt lgkmcnt(4)
	v_mfma_f32_16x16x32_f16 v[82:85], v[130:133], v[150:153], v[82:85]
	v_mfma_f32_16x16x32_f16 v[130:133], v[142:145], v[150:153], v[118:121]
	v_mfma_f32_16x16x32_f16 v[188:191], v[154:157], v[150:153], v[122:125]
	ds_read_b128 v[192:195], v186 offset:33792
	v_mfma_f32_16x16x32_f16 v[202:205], v[158:161], v[150:153], v[62:65]
	s_waitcnt lgkmcnt(4)
	v_mfma_f32_16x16x32_f16 v[206:209], v[162:165], v[134:137], v[54:57]
	s_waitcnt lgkmcnt(3)
	v_mfma_f32_16x16x32_f16 v[210:213], v[166:169], v[134:137], v[58:61]
	ds_read_b128 v[214:217], v186 offset:35840
	s_waitcnt lgkmcnt(3)
	v_mfma_f32_16x16x32_f16 v[218:221], v[170:173], v[134:137], v[42:45]
	s_waitcnt lgkmcnt(2)
	v_mfma_f32_16x16x32_f16 v[134:137], v[114:117], v[134:137], v[46:49]
	v_mfma_f32_16x16x32_f16 v[222:225], v[162:165], v[138:141], v[50:53]
	ds_read_b128 v[226:229], v186 offset:37888
	v_mfma_f32_16x16x32_f16 v[30:33], v[166:169], v[138:141], v[30:33]
	v_mfma_f32_16x16x32_f16 v[230:233], v[170:173], v[138:141], v[34:37]
	v_mfma_f32_16x16x32_f16 v[138:141], v[114:117], v[138:141], v[38:41]
	s_nop 1
	ds_read_b128 v[34:37], v186 offset:39936
	v_mfma_f32_16x16x32_f16 v[18:21], v[162:165], v[146:149], v[18:21]
	v_mfma_f32_16x16x32_f16 v[22:25], v[166:169], v[146:149], v[22:25]
	v_mfma_f32_16x16x32_f16 v[234:237], v[170:173], v[146:149], v[26:29]
	s_nop 2
	ds_read_b128 v[26:29], v187 offset:35904
	v_mfma_f32_16x16x32_f16 v[6:9], v[114:117], v[146:149], v[6:9]
	v_mfma_f32_16x16x32_f16 v[10:13], v[162:165], v[150:153], v[10:13]
	v_mfma_f32_16x16x32_f16 v[14:17], v[166:169], v[150:153], v[14:17]
	ds_read_b128 v[162:165], v187 offset:38080
	v_mfma_f32_16x16x32_f16 v[2:5], v[170:173], v[150:153], v[2:5]
	v_mfma_f32_16x16x32_f16 v[126:129], v[114:117], v[150:153], v[126:129]
	s_waitcnt lgkmcnt(1)
	v_mfma_f32_16x16x32_f16 v[158:161], v[192:195], v[26:29], v[66:69]
	ds_read_b128 v[166:169], v187 offset:40256
	v_mfma_f32_16x16x32_f16 v[154:157], v[214:217], v[26:29], v[86:89]
	v_mfma_f32_16x16x32_f16 v[150:153], v[226:229], v[26:29], v[90:93]
	v_mfma_f32_16x16x32_f16 v[146:149], v[34:37], v[26:29], v[70:73]
	s_nop 0
	ds_read_b128 v[86:89], v187 offset:42432
	s_waitcnt lgkmcnt(2)
	v_mfma_f32_16x16x32_f16 v[142:145], v[192:195], v[162:165], v[94:97]
	v_mfma_f32_16x16x32_f16 v[122:125], v[214:217], v[162:165], v[98:101]
	v_mfma_f32_16x16x32_f16 v[118:121], v[226:229], v[162:165], v[74:77]
	s_nop 0
	ds_read_b128 v[94:97], v186 offset:41984
	v_mfma_f32_16x16x32_f16 v[114:117], v[34:37], v[162:165], v[102:105]
	s_waitcnt lgkmcnt(2)
	v_mfma_f32_16x16x32_f16 v[62:65], v[192:195], v[166:169], v[106:109]
	v_mfma_f32_16x16x32_f16 v[58:61], v[214:217], v[166:169], v[78:81]
	ds_read_b128 v[98:101], v186 offset:44032
	v_mfma_f32_16x16x32_f16 v[54:57], v[226:229], v[166:169], v[110:113]
	v_mfma_f32_16x16x32_f16 v[50:53], v[34:37], v[166:169], v[174:177]
	s_waitcnt lgkmcnt(2)
	v_mfma_f32_16x16x32_f16 v[46:49], v[192:195], v[86:89], v[82:85]
	ds_read_b128 v[102:105], v186 offset:46080
	v_mfma_f32_16x16x32_f16 v[42:45], v[214:217], v[86:89], v[130:133]
	v_mfma_f32_16x16x32_f16 v[38:41], v[226:229], v[86:89], v[188:191]
	v_mfma_f32_16x16x32_f16 v[34:37], v[34:37], v[86:89], v[202:205]
	s_nop 0
	ds_read_b128 v[130:133], v186 offset:48128
	s_waitcnt lgkmcnt(3)
	v_mfma_f32_16x16x32_f16 v[110:113], v[94:97], v[26:29], v[206:209]
	s_waitcnt lgkmcnt(2)
	v_mfma_f32_16x16x32_f16 v[106:109], v[98:101], v[26:29], v[210:213]
	s_waitcnt lgkmcnt(1)
	v_mfma_f32_16x16x32_f16 v[90:93], v[102:105], v[26:29], v[218:221]
	s_waitcnt lgkmcnt(0)
	v_mfma_f32_16x16x32_f16 v[82:85], v[130:133], v[26:29], v[134:137]
	v_mfma_f32_16x16x32_f16 v[78:81], v[94:97], v[162:165], v[222:225]
	v_mfma_f32_16x16x32_f16 v[74:77], v[98:101], v[162:165], v[30:33]
	v_mfma_f32_16x16x32_f16 v[70:73], v[102:105], v[162:165], v[230:233]
	v_mfma_f32_16x16x32_f16 v[66:69], v[130:133], v[162:165], v[138:141]
	v_mfma_f32_16x16x32_f16 v[30:33], v[94:97], v[166:169], v[18:21]
	v_mfma_f32_16x16x32_f16 v[26:29], v[98:101], v[166:169], v[22:25]
	v_mfma_f32_16x16x32_f16 v[22:25], v[102:105], v[166:169], v[234:237]
	v_mfma_f32_16x16x32_f16 v[18:21], v[130:133], v[166:169], v[6:9]
	v_mfma_f32_16x16x32_f16 v[10:13], v[94:97], v[86:89], v[10:13]
	v_mfma_f32_16x16x32_f16 v[6:9], v[98:101], v[86:89], v[14:17]
	v_mfma_f32_16x16x32_f16 v[2:5], v[102:105], v[86:89], v[2:5]
	v_mfma_f32_16x16x32_f16 v[14:17], v[130:133], v[86:89], v[126:129]
	v_lshlrev_b32_e32 v86, 2, v198
	s_lshl_b32 s0, s31, 9
	v_lshl_add_u32 v86, s33, 2, v86
	v_lshl_or_b32 v172, v199, 4, s0
	v_add_u32_e32 v98, 0x22800, v86
	v_or_b32_e32 v86, 0x22000, v172
	v_or_b32_e32 v87, 0x22400, v172
	s_waitcnt vmcnt(0) lgkmcnt(0)
	s_barrier
	ds_read2_b32 v[196:197], v98 offset1:16
	ds_read_b128 v[130:133], v86
	ds_read_b128 v[86:89], v87
	v_or_b32_e32 v94, 0x22040, v172
	v_or_b32_e32 v95, 0x22440, v172
	ds_read_b128 v[126:129], v94
	ds_read_b128 v[94:97], v95
	ds_read2_b32 v[162:163], v98 offset0:32 offset1:48
	v_or_b32_e32 v102, 0x22500, v172
	s_waitcnt lgkmcnt(3)
	v_pk_mul_f32 v[186:187], v[130:131], v[86:87]
	v_or_b32_e32 v86, 0x22080, v172
	s_waitcnt lgkmcnt(1)
	v_pk_mul_f32 v[180:181], v[128:129], v[96:97]
	v_pk_mul_f32 v[182:183], v[126:127], v[94:95]
	v_or_b32_e32 v87, 0x22480, v172
	ds_read_b128 v[134:137], v86
	ds_read_b128 v[94:97], v87
	v_or_b32_e32 v86, 0x220c0, v172
	v_or_b32_e32 v87, 0x224c0, v172
	ds_read_b128 v[138:141], v86
	ds_read_b128 v[98:101], v87
	v_or_b32_e32 v86, 0x22100, v172
	v_pk_mul_f32 v[184:185], v[132:133], v[88:89]
	ds_read_b128 v[86:89], v86
	ds_read_b128 v[102:105], v102
	s_mulk_i32 s30, 0x2200
	s_waitcnt lgkmcnt(4)
	v_pk_mul_f32 v[192:193], v[136:137], v[96:97]
	v_pk_mul_f32 v[194:195], v[134:135], v[94:95]
	s_waitcnt lgkmcnt(2)
	v_pk_mul_f32 v[188:189], v[140:141], v[100:101]
	v_pk_mul_f32 v[190:191], v[138:139], v[98:99]
	v_or_b32_e32 v94, 0x22140, v172
	v_or_b32_e32 v98, 0x22540, v172
	v_and_or_b32 v0, v0, 48, s30
	s_movk_i32 s2, 0x110
	s_waitcnt lgkmcnt(0)
	v_pk_mul_f32 v[166:167], v[86:87], v[102:103]
	ds_read_b128 v[94:97], v94
	ds_read_b128 v[168:171], v98
	v_or_b32_e32 v98, 0x22180, v172
	v_or_b32_e32 v102, 0x22580, v172
	v_mad_u32_u24 v198, v198, s2, v0
	v_pk_fma_f32 v[160:161], v[160:161], v[132:133], v[184:185]
	v_pk_fma_f32 v[158:159], v[158:159], v[130:131], v[186:187]
	v_pk_fma_f32 v[156:157], v[156:157], v[128:129], v[180:181]
	v_pk_fma_f32 v[154:155], v[154:155], v[126:127], v[182:183]
	v_pk_fma_f32 v[152:153], v[152:153], v[136:137], v[192:193]
	v_pk_fma_f32 v[150:151], v[150:151], v[134:135], v[194:195]
	v_pk_fma_f32 v[148:149], v[148:149], v[140:141], v[188:189]
	v_pk_fma_f32 v[146:147], v[146:147], v[138:139], v[190:191]
	v_pk_fma_f32 v[144:145], v[144:145], v[132:133], v[184:185]
	v_pk_fma_f32 v[142:143], v[142:143], v[130:131], v[186:187]
	v_mov_b32_e32 v0, v197
	v_pk_fma_f32 v[124:125], v[124:125], v[128:129], v[180:181]
	v_pk_fma_f32 v[122:123], v[122:123], v[126:127], v[182:183]
	v_pk_fma_f32 v[120:121], v[120:121], v[136:137], v[192:193]
	v_pk_fma_f32 v[118:119], v[118:119], v[134:135], v[194:195]
	v_pk_fma_f32 v[116:117], v[116:117], v[140:141], v[188:189]
	v_pk_fma_f32 v[114:115], v[114:115], v[138:139], v[190:191]
	ds_read_b128 v[98:101], v98
	ds_read_b128 v[202:205], v102
	v_or_b32_e32 v102, 0x221c0, v172
	v_or_b32_e32 v200, s30, v200
	v_pk_mul_f32 v[160:161], v[160:161], v[196:197] op_sel_hi:[1,0]
	v_pk_mul_f32 v[158:159], v[158:159], v[196:197] op_sel_hi:[1,0]
	v_pk_mul_f32 v[156:157], v[156:157], v[196:197] op_sel_hi:[1,0]
	v_pk_mul_f32 v[154:155], v[154:155], v[196:197] op_sel_hi:[1,0]
	v_pk_mul_f32 v[152:153], v[152:153], v[196:197] op_sel_hi:[1,0]
	v_pk_mul_f32 v[150:151], v[150:151], v[196:197] op_sel_hi:[1,0]
	v_pk_mul_f32 v[148:149], v[148:149], v[196:197] op_sel_hi:[1,0]
	v_pk_mul_f32 v[146:147], v[146:147], v[196:197] op_sel_hi:[1,0]
	v_pk_mul_f32 v[144:145], v[144:145], v[0:1] op_sel_hi:[1,0]
	v_pk_mul_f32 v[142:143], v[142:143], v[0:1] op_sel_hi:[1,0]
	v_pk_mul_f32 v[124:125], v[124:125], v[0:1] op_sel_hi:[1,0]
	v_pk_mul_f32 v[122:123], v[122:123], v[0:1] op_sel_hi:[1,0]
	v_pk_mul_f32 v[120:121], v[120:121], v[0:1] op_sel_hi:[1,0]
	v_pk_mul_f32 v[118:119], v[118:119], v[0:1] op_sel_hi:[1,0]
	v_pk_mul_f32 v[116:117], v[116:117], v[0:1] op_sel_hi:[1,0]
	v_pk_mul_f32 v[114:115], v[114:115], v[0:1] op_sel_hi:[1,0]
	v_pk_mul_f32 v[164:165], v[88:89], v[104:105]
	v_or_b32_e32 v172, 0x225c0, v172
	ds_read_b128 v[102:105], v102
	ds_read_b128 v[206:209], v172
	v_mad_u32_u24 v199, v199, s2, v200
	ds_write_b128 v198, v[158:161]
	ds_write_b128 v198, v[154:157] offset:64
	ds_write_b128 v198, v[150:153] offset:128
	ds_write_b128 v198, v[146:149] offset:192
	ds_write_b128 v198, v[142:145] offset:4352
	ds_write_b128 v198, v[122:125] offset:4416
	ds_write_b128 v198, v[118:121] offset:4480
	ds_write_b128 v198, v[114:117] offset:4544
	ds_read_b128 v[114:117], v199
	ds_read_b128 v[118:121], v199 offset:1088
	s_lshl_b32 s1, s29, 2
	s_lshl_b32 s2, s28, 12
	s_or_b32 s1, s2, s1
	s_and_b32 s9, s9, 0xffff
	s_mov_b32 s11, 0x20000
	s_brev_b32 s10, 16
	s_or_b32 s0, s0, s1
	s_waitcnt lgkmcnt(1)
	buffer_store_dwordx4 v[114:117], v1, s[8:11], s0 offen nt
	ds_read_b128 v[114:117], v199 offset:2176
	s_or_b32 s1, s0, 0x4000
	s_waitcnt lgkmcnt(1)
	buffer_store_dwordx4 v[118:121], v1, s[8:11], s1 offen nt
	ds_read_b128 v[118:121], v199 offset:3264
	s_or_b32 s1, s0, 0x8000
	s_waitcnt lgkmcnt(1)
	buffer_store_dwordx4 v[114:117], v1, s[8:11], s1 offen nt
	ds_read_b128 v[114:117], v199 offset:4352
	s_or_b32 s1, s0, 0xc000
	s_waitcnt lgkmcnt(1)
	buffer_store_dwordx4 v[118:121], v1, s[8:11], s1 offen nt
	ds_read_b128 v[118:121], v199 offset:5440
	v_pk_mul_f32 v[176:177], v[96:97], v[170:171]
	v_pk_mul_f32 v[178:179], v[94:95], v[168:169]
	v_pk_mul_f32 v[172:173], v[100:101], v[204:205]
	v_pk_mul_f32 v[174:175], v[98:99], v[202:203]
	v_pk_mul_f32 v[168:169], v[104:105], v[208:209]
	v_pk_mul_f32 v[170:171], v[102:103], v[206:207]
	s_or_b32 s1, s0, 0x10000
	v_pk_fma_f32 v[112:113], v[112:113], v[88:89], v[164:165]
	v_pk_fma_f32 v[110:111], v[110:111], v[86:87], v[166:167]
	v_pk_fma_f32 v[108:109], v[108:109], v[96:97], v[176:177]
	v_pk_fma_f32 v[106:107], v[106:107], v[94:95], v[178:179]
	v_pk_fma_f32 v[92:93], v[92:93], v[100:101], v[172:173]
	v_pk_fma_f32 v[90:91], v[90:91], v[98:99], v[174:175]
	v_pk_fma_f32 v[84:85], v[84:85], v[104:105], v[168:169]
	v_pk_fma_f32 v[82:83], v[82:83], v[102:103], v[170:171]
	v_pk_fma_f32 v[80:81], v[80:81], v[88:89], v[164:165]
	v_pk_fma_f32 v[78:79], v[78:79], v[86:87], v[166:167]
	v_pk_fma_f32 v[76:77], v[76:77], v[96:97], v[176:177]
	v_pk_fma_f32 v[74:75], v[74:75], v[94:95], v[178:179]
	v_pk_fma_f32 v[72:73], v[72:73], v[100:101], v[172:173]
	v_pk_fma_f32 v[70:71], v[70:71], v[98:99], v[174:175]
	v_pk_fma_f32 v[68:69], v[68:69], v[104:105], v[168:169]
	v_pk_fma_f32 v[66:67], v[66:67], v[102:103], v[170:171]
	s_waitcnt lgkmcnt(1)
	buffer_store_dwordx4 v[114:117], v1, s[8:11], s1 offen nt
	ds_read_b128 v[114:117], v199 offset:6528
	s_or_b32 s1, s0, 0x14000
	v_pk_mul_f32 v[112:113], v[112:113], v[196:197] op_sel_hi:[1,0]
	v_pk_mul_f32 v[110:111], v[110:111], v[196:197] op_sel_hi:[1,0]
	v_pk_mul_f32 v[108:109], v[108:109], v[196:197] op_sel_hi:[1,0]
	v_pk_mul_f32 v[106:107], v[106:107], v[196:197] op_sel_hi:[1,0]
	v_pk_mul_f32 v[92:93], v[92:93], v[196:197] op_sel_hi:[1,0]
	v_pk_mul_f32 v[90:91], v[90:91], v[196:197] op_sel_hi:[1,0]
	v_pk_mul_f32 v[84:85], v[84:85], v[196:197] op_sel_hi:[1,0]
	v_pk_mul_f32 v[82:83], v[82:83], v[196:197] op_sel_hi:[1,0]
	v_pk_mul_f32 v[80:81], v[80:81], v[0:1] op_sel_hi:[1,0]
	v_pk_mul_f32 v[78:79], v[78:79], v[0:1] op_sel_hi:[1,0]
	v_pk_mul_f32 v[76:77], v[76:77], v[0:1] op_sel_hi:[1,0]
	v_pk_mul_f32 v[74:75], v[74:75], v[0:1] op_sel_hi:[1,0]
	v_pk_mul_f32 v[72:73], v[72:73], v[0:1] op_sel_hi:[1,0]
	v_pk_mul_f32 v[70:71], v[70:71], v[0:1] op_sel_hi:[1,0]
	v_pk_mul_f32 v[68:69], v[68:69], v[0:1] op_sel_hi:[1,0]
	v_pk_mul_f32 v[66:67], v[66:67], v[0:1] op_sel_hi:[1,0]
	s_waitcnt lgkmcnt(1)
	buffer_store_dwordx4 v[118:121], v1, s[8:11], s1 offen nt
	ds_read_b128 v[118:121], v199 offset:7616
	ds_write_b128 v198, v[110:113]
	ds_write_b128 v198, v[106:109] offset:64
	ds_write_b128 v198, v[90:93] offset:128
	ds_write_b128 v198, v[82:85] offset:192
	ds_write_b128 v198, v[78:81] offset:4352
	ds_write_b128 v198, v[74:77] offset:4416
	ds_write_b128 v198, v[70:73] offset:4480
	ds_write_b128 v198, v[66:69] offset:4544
	ds_read_b128 v[66:69], v199
	ds_read_b128 v[70:73], v199 offset:1088
	s_or_b32 s1, s0, 0x18000
	s_waitcnt lgkmcnt(11)
	buffer_store_dwordx4 v[114:117], v1, s[8:11], s1 offen nt
	s_or_b32 s1, s0, 0x1c000
	s_waitcnt lgkmcnt(10)
	buffer_store_dwordx4 v[118:121], v1, s[8:11], s1 offen nt
	s_or_b32 s1, s0, 0x100
	s_waitcnt lgkmcnt(1)
	buffer_store_dwordx4 v[66:69], v1, s[8:11], s1 offen nt
	ds_read_b128 v[66:69], v199 offset:2176
	s_or_b32 s1, s0, 0x4100
	s_waitcnt lgkmcnt(1)
	buffer_store_dwordx4 v[70:73], v1, s[8:11], s1 offen nt
	ds_read_b128 v[70:73], v199 offset:3264
	s_or_b32 s1, s0, 0x8100
	s_waitcnt lgkmcnt(1)
	buffer_store_dwordx4 v[66:69], v1, s[8:11], s1 offen nt
	ds_read_b128 v[66:69], v199 offset:4352
	s_or_b32 s1, s0, 0xc100
	s_waitcnt lgkmcnt(1)
	buffer_store_dwordx4 v[70:73], v1, s[8:11], s1 offen nt
	ds_read_b128 v[70:73], v199 offset:5440
	s_or_b32 s1, s0, 0x10100
	v_pk_fma_f32 v[64:65], v[64:65], v[132:133], v[184:185]
	v_pk_fma_f32 v[62:63], v[62:63], v[130:131], v[186:187]
	v_pk_fma_f32 v[60:61], v[60:61], v[128:129], v[180:181]
	v_pk_fma_f32 v[58:59], v[58:59], v[126:127], v[182:183]
	v_pk_fma_f32 v[56:57], v[56:57], v[136:137], v[192:193]
	v_pk_fma_f32 v[54:55], v[54:55], v[134:135], v[194:195]
	v_pk_fma_f32 v[52:53], v[52:53], v[140:141], v[188:189]
	v_pk_fma_f32 v[50:51], v[50:51], v[138:139], v[190:191]
	v_pk_fma_f32 v[48:49], v[48:49], v[132:133], v[184:185]
	v_pk_fma_f32 v[46:47], v[46:47], v[130:131], v[186:187]
	v_mov_b32_e32 v0, v163
	v_pk_fma_f32 v[44:45], v[44:45], v[128:129], v[180:181]
	v_pk_fma_f32 v[42:43], v[42:43], v[126:127], v[182:183]
	v_pk_fma_f32 v[40:41], v[40:41], v[136:137], v[192:193]
	v_pk_fma_f32 v[38:39], v[38:39], v[134:135], v[194:195]
	v_pk_fma_f32 v[36:37], v[36:37], v[140:141], v[188:189]
	v_pk_fma_f32 v[34:35], v[34:35], v[138:139], v[190:191]
	s_waitcnt lgkmcnt(1)
	buffer_store_dwordx4 v[66:69], v1, s[8:11], s1 offen nt
	ds_read_b128 v[66:69], v199 offset:6528
	s_or_b32 s1, s0, 0x14100
	v_pk_mul_f32 v[64:65], v[64:65], v[162:163] op_sel_hi:[1,0]
	v_pk_mul_f32 v[62:63], v[62:63], v[162:163] op_sel_hi:[1,0]
	v_pk_mul_f32 v[60:61], v[60:61], v[162:163] op_sel_hi:[1,0]
	v_pk_mul_f32 v[58:59], v[58:59], v[162:163] op_sel_hi:[1,0]
	v_pk_mul_f32 v[56:57], v[56:57], v[162:163] op_sel_hi:[1,0]
	v_pk_mul_f32 v[54:55], v[54:55], v[162:163] op_sel_hi:[1,0]
	v_pk_mul_f32 v[52:53], v[52:53], v[162:163] op_sel_hi:[1,0]
	v_pk_mul_f32 v[50:51], v[50:51], v[162:163] op_sel_hi:[1,0]
	v_pk_mul_f32 v[48:49], v[48:49], v[0:1] op_sel_hi:[1,0]
	v_pk_mul_f32 v[46:47], v[46:47], v[0:1] op_sel_hi:[1,0]
	v_pk_mul_f32 v[44:45], v[44:45], v[0:1] op_sel_hi:[1,0]
	v_pk_mul_f32 v[42:43], v[42:43], v[0:1] op_sel_hi:[1,0]
	v_pk_mul_f32 v[40:41], v[40:41], v[0:1] op_sel_hi:[1,0]
	v_pk_mul_f32 v[38:39], v[38:39], v[0:1] op_sel_hi:[1,0]
	v_pk_mul_f32 v[36:37], v[36:37], v[0:1] op_sel_hi:[1,0]
	v_pk_mul_f32 v[34:35], v[34:35], v[0:1] op_sel_hi:[1,0]
	s_waitcnt lgkmcnt(1)
	buffer_store_dwordx4 v[70:73], v1, s[8:11], s1 offen nt
	ds_read_b128 v[70:73], v199 offset:7616
	ds_write_b128 v198, v[62:65]
	ds_write_b128 v198, v[58:61] offset:64
	ds_write_b128 v198, v[54:57] offset:128
	ds_write_b128 v198, v[50:53] offset:192
	ds_write_b128 v198, v[46:49] offset:4352
	ds_write_b128 v198, v[42:45] offset:4416
	ds_write_b128 v198, v[38:41] offset:4480
	ds_write_b128 v198, v[34:37] offset:4544
	ds_read_b128 v[34:37], v199
	ds_read_b128 v[38:41], v199 offset:1088
	s_or_b32 s1, s0, 0x18100
	s_waitcnt lgkmcnt(11)
	buffer_store_dwordx4 v[66:69], v1, s[8:11], s1 offen nt
	s_or_b32 s1, s0, 0x1c100
	s_waitcnt lgkmcnt(10)
	buffer_store_dwordx4 v[70:73], v1, s[8:11], s1 offen nt
	s_or_b32 s1, s0, 0x20000
	s_waitcnt lgkmcnt(1)
	buffer_store_dwordx4 v[34:37], v1, s[8:11], s1 offen nt
	ds_read_b128 v[34:37], v199 offset:2176
	s_or_b32 s1, s0, 0x24000
	s_waitcnt lgkmcnt(1)
	buffer_store_dwordx4 v[38:41], v1, s[8:11], s1 offen nt
	ds_read_b128 v[38:41], v199 offset:3264
	s_or_b32 s1, s0, 0x28000
	s_waitcnt lgkmcnt(1)
	buffer_store_dwordx4 v[34:37], v1, s[8:11], s1 offen nt
	ds_read_b128 v[34:37], v199 offset:4352
	s_or_b32 s1, s0, 0x2c000
	s_waitcnt lgkmcnt(1)
	buffer_store_dwordx4 v[38:41], v1, s[8:11], s1 offen nt
	ds_read_b128 v[38:41], v199 offset:5440
	s_or_b32 s1, s0, 0x30000
	v_pk_fma_f32 v[8:9], v[8:9], v[96:97], v[176:177]
	v_pk_fma_f32 v[6:7], v[6:7], v[94:95], v[178:179]
	v_pk_fma_f32 v[4:5], v[4:5], v[100:101], v[172:173]
	v_pk_fma_f32 v[2:3], v[2:3], v[98:99], v[174:175]
	s_waitcnt lgkmcnt(1)
	buffer_store_dwordx4 v[34:37], v1, s[8:11], s1 offen nt
	s_or_b32 s1, s0, 0x34000
	v_pk_mul_f32 v[8:9], v[8:9], v[0:1] op_sel_hi:[1,0]
	v_pk_mul_f32 v[6:7], v[6:7], v[0:1] op_sel_hi:[1,0]
	v_pk_mul_f32 v[4:5], v[4:5], v[0:1] op_sel_hi:[1,0]
	v_pk_mul_f32 v[2:3], v[2:3], v[0:1] op_sel_hi:[1,0]
	ds_read_b128 v[34:37], v199 offset:6528
	s_waitcnt lgkmcnt(1)
	buffer_store_dwordx4 v[38:41], v1, s[8:11], s1 offen nt
	ds_read_b128 v[38:41], v199 offset:7616
	v_pk_fma_f32 v[32:33], v[32:33], v[88:89], v[164:165]
	v_pk_fma_f32 v[30:31], v[30:31], v[86:87], v[166:167]
	v_pk_fma_f32 v[28:29], v[28:29], v[96:97], v[176:177]
	v_pk_fma_f32 v[26:27], v[26:27], v[94:95], v[178:179]
	v_pk_fma_f32 v[24:25], v[24:25], v[100:101], v[172:173]
	v_pk_fma_f32 v[22:23], v[22:23], v[98:99], v[174:175]
	v_pk_fma_f32 v[20:21], v[20:21], v[104:105], v[168:169]
	v_pk_fma_f32 v[18:19], v[18:19], v[102:103], v[170:171]
	v_pk_fma_f32 v[12:13], v[12:13], v[88:89], v[164:165]
	v_pk_fma_f32 v[10:11], v[10:11], v[86:87], v[166:167]
	ds_write_b128 v198, v[6:9] offset:4416
	ds_write_b128 v198, v[2:5] offset:4480
	v_pk_fma_f32 v[2:3], v[16:17], v[104:105], v[168:169]
	v_pk_fma_f32 v[6:7], v[14:15], v[102:103], v[170:171]
	v_pk_mul_f32 v[32:33], v[32:33], v[162:163] op_sel_hi:[1,0]
	v_pk_mul_f32 v[30:31], v[30:31], v[162:163] op_sel_hi:[1,0]
	v_pk_mul_f32 v[28:29], v[28:29], v[162:163] op_sel_hi:[1,0]
	v_pk_mul_f32 v[26:27], v[26:27], v[162:163] op_sel_hi:[1,0]
	v_pk_mul_f32 v[24:25], v[24:25], v[162:163] op_sel_hi:[1,0]
	v_pk_mul_f32 v[22:23], v[22:23], v[162:163] op_sel_hi:[1,0]
	v_pk_mul_f32 v[20:21], v[20:21], v[162:163] op_sel_hi:[1,0]
	v_pk_mul_f32 v[18:19], v[18:19], v[162:163] op_sel_hi:[1,0]
	v_pk_mul_f32 v[12:13], v[12:13], v[0:1] op_sel_hi:[1,0]
	v_pk_mul_f32 v[10:11], v[10:11], v[0:1] op_sel_hi:[1,0]
	v_pk_mul_f32 v[4:5], v[2:3], v[0:1] op_sel_hi:[1,0]
	v_pk_mul_f32 v[2:3], v[6:7], v[0:1] op_sel_hi:[1,0]
	ds_write_b128 v198, v[30:33]
	ds_write_b128 v198, v[26:29] offset:64
	ds_write_b128 v198, v[22:25] offset:128
	ds_write_b128 v198, v[18:21] offset:192
	ds_write_b128 v198, v[10:13] offset:4352
	ds_write_b128 v198, v[2:5] offset:4544
	ds_read_b128 v[2:5], v199
	s_or_b32 s1, s0, 0x38000
	s_waitcnt lgkmcnt(10)
	buffer_store_dwordx4 v[34:37], v1, s[8:11], s1 offen nt
	s_or_b32 s1, s0, 0x3c000
	s_waitcnt lgkmcnt(9)
	buffer_store_dwordx4 v[38:41], v1, s[8:11], s1 offen nt
	ds_read_b128 v[6:9], v199 offset:1088
	s_or_b32 s1, s0, 0x20100
	s_waitcnt lgkmcnt(1)
	buffer_store_dwordx4 v[2:5], v1, s[8:11], s1 offen nt
	ds_read_b128 v[2:5], v199 offset:2176
	s_or_b32 s1, s0, 0x24100
	s_waitcnt lgkmcnt(1)
	buffer_store_dwordx4 v[6:9], v1, s[8:11], s1 offen nt
	ds_read_b128 v[6:9], v199 offset:3264
	s_or_b32 s1, s0, 0x28100
	s_waitcnt lgkmcnt(1)
	buffer_store_dwordx4 v[2:5], v1, s[8:11], s1 offen nt
	ds_read_b128 v[2:5], v199 offset:4352
	s_or_b32 s1, s0, 0x2c100
	s_waitcnt lgkmcnt(1)
	buffer_store_dwordx4 v[6:9], v1, s[8:11], s1 offen nt
	s_or_b32 s1, s0, 0x30100
	ds_read_b128 v[6:9], v199 offset:5440
	s_waitcnt lgkmcnt(1)
	buffer_store_dwordx4 v[2:5], v1, s[8:11], s1 offen nt
	ds_read_b128 v[2:5], v199 offset:6528
	ds_read_b128 v[10:13], v199 offset:7616
	s_or_b32 s1, s0, 0x34100
	s_waitcnt lgkmcnt(2)
	buffer_store_dwordx4 v[6:9], v1, s[8:11], s1 offen nt
	s_or_b32 s1, s0, 0x38100
	s_or_b32 s0, s0, 0x3c100
	s_waitcnt lgkmcnt(1)
	buffer_store_dwordx4 v[2:5], v1, s[8:11], s1 offen nt
	s_waitcnt lgkmcnt(0)
	buffer_store_dwordx4 v[10:13], v1, s[8:11], s0 offen nt
	s_endpgm
